# baseline (speedup 1.0000x reference)
_Z12final_kernelPKDv4_fS1_PKfS3_Pf:
	s_load_dwordx4 s[4:7], s[0:1], 0x0
	s_load_dwordx2 s[2:3], s[0:1], 0x10
	s_load_dwordx2 s[8:9], s[0:1], 0x20
	v_and_b32_e32 v1, 0x1ff, v0
	v_readfirstlane_b32 s10, v0
	v_lshlrev_b32_e32 v2, 4, v1
	v_lshlrev_b32_e32 v3, 2, v1
	v_add_u32_e32 v4, 0x2000, v2
	v_add_u32_e32 v5, 0x4000, v2
	v_add_u32_e32 v6, 0x6000, v2
	v_add_u32_e32 v7, 0x8000, v2
	v_add_u32_e32 v8, 0xa000, v2
	v_add_u32_e32 v9, 0xc000, v2
	v_add_u32_e32 v10, 0xe000, v2
	s_cmpk_ge_u32 s10, 0x200
	s_waitcnt lgkmcnt(0)
	s_cselect_b32 s4, s6, s4
	s_cselect_b32 s5, s7, s5
	global_load_dwordx4 v[12:15], v2, s[4:5]
	global_load_dwordx4 v[16:19], v4, s[4:5]
	global_load_dwordx4 v[20:23], v5, s[4:5]
	global_load_dwordx4 v[24:27], v6, s[4:5]
	global_load_dwordx4 v[28:31], v7, s[4:5]
	global_load_dwordx4 v[32:35], v8, s[4:5]
	global_load_dwordx4 v[36:39], v9, s[4:5]
	global_load_dwordx4 v[40:43], v10, s[4:5]
	global_load_dword v44, v3, s[2:3]
	global_load_dword v45, v3, s[2:3] offset:2048
	s_waitcnt vmcnt(2)
	v_max3_f32 v46, v12, v14, v16
	v_max3_f32 v47, v18, v20, v22
	v_max3_f32 v48, v24, v26, v28
	v_max3_f32 v49, v30, v32, v34
	v_max3_f32 v46, v46, v36, v38
	v_max3_f32 v47, v47, v40, v42
	v_max3_f32 v46, v46, v48, v49
	v_max_f32_e32 v46, v46, v47
	v_sub_f32_e32 v12, v12, v46
	v_sub_f32_e32 v14, v14, v46
	v_sub_f32_e32 v16, v16, v46
	v_sub_f32_e32 v18, v18, v46
	v_sub_f32_e32 v20, v20, v46
	v_sub_f32_e32 v22, v22, v46
	v_sub_f32_e32 v24, v24, v46
	v_sub_f32_e32 v26, v26, v46
	v_sub_f32_e32 v28, v28, v46
	v_sub_f32_e32 v30, v30, v46
	v_sub_f32_e32 v32, v32, v46
	v_sub_f32_e32 v34, v34, v46
	v_sub_f32_e32 v36, v36, v46
	v_sub_f32_e32 v38, v38, v46
	v_sub_f32_e32 v40, v40, v46
	v_sub_f32_e32 v42, v42, v46
	v_mul_f32_e32 v12, 0x3fb8aa3b, v12
	v_mul_f32_e32 v14, 0x3fb8aa3b, v14
	v_mul_f32_e32 v16, 0x3fb8aa3b, v16
	v_mul_f32_e32 v18, 0x3fb8aa3b, v18
	v_mul_f32_e32 v20, 0x3fb8aa3b, v20
	v_mul_f32_e32 v22, 0x3fb8aa3b, v22
	v_mul_f32_e32 v24, 0x3fb8aa3b, v24
	v_mul_f32_e32 v26, 0x3fb8aa3b, v26
	v_mul_f32_e32 v28, 0x3fb8aa3b, v28
	v_mul_f32_e32 v30, 0x3fb8aa3b, v30
	v_mul_f32_e32 v32, 0x3fb8aa3b, v32
	v_mul_f32_e32 v34, 0x3fb8aa3b, v34
	v_mul_f32_e32 v36, 0x3fb8aa3b, v36
	v_mul_f32_e32 v38, 0x3fb8aa3b, v38
	v_mul_f32_e32 v40, 0x3fb8aa3b, v40
	v_mul_f32_e32 v42, 0x3fb8aa3b, v42
	v_exp_f32_e32 v12, v12
	v_exp_f32_e32 v14, v14
	v_exp_f32_e32 v16, v16
	v_exp_f32_e32 v18, v18
	v_exp_f32_e32 v20, v20
	v_exp_f32_e32 v22, v22
	v_exp_f32_e32 v24, v24
	v_exp_f32_e32 v26, v26
	v_exp_f32_e32 v28, v28
	v_exp_f32_e32 v30, v30
	v_exp_f32_e32 v32, v32
	v_exp_f32_e32 v34, v34
	v_exp_f32_e32 v36, v36
	v_exp_f32_e32 v38, v38
	v_exp_f32_e32 v40, v40
	v_exp_f32_e32 v42, v42
	s_nop 0
	v_mul_f32_e32 v47, v13, v12
	v_mul_f32_e32 v48, v17, v16
	v_mul_f32_e32 v49, v21, v20
	v_mul_f32_e32 v50, v25, v24
	v_fmac_f32_e32 v47, v15, v14
	v_fmac_f32_e32 v48, v19, v18
	v_fmac_f32_e32 v49, v23, v22
	v_fmac_f32_e32 v50, v27, v26
	v_fmac_f32_e32 v47, v29, v28
	v_fmac_f32_e32 v48, v33, v32
	v_fmac_f32_e32 v49, v37, v36
	v_fmac_f32_e32 v50, v41, v40
	v_fmac_f32_e32 v47, v31, v30
	v_fmac_f32_e32 v48, v35, v34
	v_fmac_f32_e32 v49, v39, v38
	v_fmac_f32_e32 v50, v43, v42
	v_add_f32_e32 v47, v47, v48
	v_add_f32_e32 v49, v49, v50
	v_add_f32_e32 v47, v47, v49
	v_log_f32_e32 v47, v47
	s_mov_b32 s11, 0x3f317217
	v_mul_f32_e32 v48, 0x3f317217, v47
	v_fma_f32 v48, v47, s11, -v48
	v_fmamk_f32 v48, v47, 0x3377d1cf, v48
	v_fmac_f32_e32 v48, 0x3f317217, v47
	v_add_f32_e32 v46, v46, v48
	s_waitcnt vmcnt(0)
	v_sub_f32_e32 v46, v46, v44
	v_cmp_lt_f32_e32 vcc, 0, v45
	s_nop 1
	v_cndmask_b32_e32 v46, 0, v46, vcc
	v_cmp_lt_f32_e32 vcc, 0, v46
	v_max_f32_e32 v2, 0, v46
	s_nop 0
	v_cndmask_b32_e64 v3, 0, 1.0, vcc
	s_nop 0
	s_nop 0
	v_add_f32_dpp v2, v2, v2 quad_perm:[1,0,3,2] row_mask:0xf bank_mask:0xf
	v_add_f32_dpp v3, v3, v3 quad_perm:[1,0,3,2] row_mask:0xf bank_mask:0xf
	s_nop 0
	v_add_f32_dpp v2, v2, v2 quad_perm:[2,3,0,1] row_mask:0xf bank_mask:0xf
	v_add_f32_dpp v3, v3, v3 quad_perm:[2,3,0,1] row_mask:0xf bank_mask:0xf
	s_nop 0
	v_add_f32_dpp v2, v2, v2 row_half_mirror row_mask:0xf bank_mask:0xf
	v_add_f32_dpp v3, v3, v3 row_half_mirror row_mask:0xf bank_mask:0xf
	s_nop 0
	v_add_f32_dpp v2, v2, v2 row_mirror row_mask:0xf bank_mask:0xf
	v_add_f32_dpp v3, v3, v3 row_mirror row_mask:0xf bank_mask:0xf
	s_nop 0
	v_add_f32_dpp v2, v2, v2 row_bcast:15 row_mask:0xa bank_mask:0xf
	v_add_f32_dpp v3, v3, v3 row_bcast:15 row_mask:0xa bank_mask:0xf
	s_nop 0
	v_add_f32_dpp v2, v2, v2 row_bcast:31 row_mask:0xc bank_mask:0xf
	v_add_f32_dpp v3, v3, v3 row_bcast:31 row_mask:0xc bank_mask:0xf
	s_nop 1
	v_readlane_b32 s12, v2, 63
	v_readlane_b32 s13, v3, 63
	s_lshr_b32 s10, s10, 6
	s_lshl_b32 s10, s10, 2
	v_mov_b32_e32 v4, s10
	v_mov_b32_e32 v5, s12
	v_mov_b32_e32 v6, s13
	ds_write2_b32 v4, v5, v6 offset1:16
	s_waitcnt lgkmcnt(0)
	s_barrier
	s_cmp_lg_u32 s10, 0
	s_cbranch_scc1 .Lfin_end
	v_and_b32_e32 v4, 15, v0
	v_lshlrev_b32_e32 v4, 2, v4
	ds_read2_b32 v[2:3], v4 offset1:16
	s_waitcnt lgkmcnt(0)
	s_nop 0
	s_nop 0
	v_add_f32_dpp v2, v2, v2 quad_perm:[1,0,3,2] row_mask:0xf bank_mask:0xf
	v_add_f32_dpp v3, v3, v3 quad_perm:[1,0,3,2] row_mask:0xf bank_mask:0xf
	s_nop 0
	v_add_f32_dpp v2, v2, v2 quad_perm:[2,3,0,1] row_mask:0xf bank_mask:0xf
	v_add_f32_dpp v3, v3, v3 quad_perm:[2,3,0,1] row_mask:0xf bank_mask:0xf
	s_nop 0
	v_add_f32_dpp v2, v2, v2 row_half_mirror row_mask:0xf bank_mask:0xf
	v_add_f32_dpp v3, v3, v3 row_half_mirror row_mask:0xf bank_mask:0xf
	v_max_f32_e32 v5, 1.0, v3
	v_div_scale_f32 v6, s[12:13], v5, v5, v2
	v_rcp_f32_e32 v7, v6
	v_div_scale_f32 v8, vcc, v2, v5, v2
	v_fma_f32 v9, -v6, v7, 1.0
	v_fmac_f32_e32 v7, v9, v7
	v_mul_f32_e32 v9, v8, v7
	v_fma_f32 v10, -v6, v9, v8
	v_fmac_f32_e32 v9, v10, v7
	v_fma_f32 v6, -v6, v9, v8
	v_div_fmas_f32 v6, v6, v7, v9
	v_div_fixup_f32 v6, v6, v5, v2
	v_cmp_lt_f32_e32 vcc, 0, v3
	s_nop 1
	v_cndmask_b32_e32 v6, 0, v6, vcc
	s_nop 1
	v_add_f32_dpp v7, v6, v6 row_shl:8 row_mask:0xf bank_mask:0xf
	v_mov_b32_e32 v8, 0
	v_mul_f32_e32 v7, 0.5, v7
	v_cmp_eq_u32_e32 vcc, 0, v0
	s_and_saveexec_b64 s[12:13], vcc
	global_store_dword v8, v7, s[8:9]

	.amdhsa_kernel _Z12final_kernelPKDv4_fS1_PKfS3_Pf
		.amdhsa_group_segment_fixed_size 128
		.amdhsa_private_segment_fixed_size 0
		.amdhsa_kernarg_size 40
		.amdhsa_user_sgpr_count 2
		.amdhsa_user_sgpr_dispatch_ptr 0
		.amdhsa_user_sgpr_queue_ptr 0
		.amdhsa_user_sgpr_kernarg_segment_ptr 1
		.amdhsa_user_sgpr_dispatch_id 0
		.amdhsa_user_sgpr_kernarg_preload_length 0
		.amdhsa_user_sgpr_kernarg_preload_offset 0
		.amdhsa_user_sgpr_private_segment_size 0
		.amdhsa_uses_dynamic_stack 0
		.amdhsa_enable_private_segment 0
		.amdhsa_system_sgpr_workgroup_id_x 1
		.amdhsa_system_sgpr_workgroup_id_y 0
		.amdhsa_system_sgpr_workgroup_id_z 0
		.amdhsa_system_sgpr_workgroup_info 0
		.amdhsa_system_vgpr_workitem_id 0
		.amdhsa_next_free_vgpr 52
		.amdhsa_next_free_sgpr 14
		.amdhsa_accum_offset 52
		.amdhsa_reserve_vcc 1
		.amdhsa_float_round_mode_32 0
		.amdhsa_float_round_mode_16_64 0
		.amdhsa_float_denorm_mode_32 3
		.amdhsa_float_denorm_mode_16_64 3
		.amdhsa_dx10_clamp 1
		.amdhsa_ieee_mode 1
		.amdhsa_fp16_overflow 0
		.amdhsa_tg_split 0
		.amdhsa_exception_fp_ieee_invalid_op 0
		.amdhsa_exception_fp_denorm_src 0
		.amdhsa_exception_fp_ieee_div_zero 0
		.amdhsa_exception_fp_ieee_overflow 0
		.amdhsa_exception_fp_ieee_underflow 0
		.amdhsa_exception_fp_ieee_inexact 0
		.amdhsa_exception_int_div_zero 0
	.end_amdhsa_kernel

amdhsa.kernels:
  - .agpr_count:     0
    .args:
      - .actual_access:  read_only
        .address_space:  global
        .offset:         0
        .size:           8
        .value_kind:     global_buffer
      - .actual_access:  read_only
        .address_space:  global
        .offset:         8
        .size:           8
        .value_kind:     global_buffer
      - .actual_access:  read_only
        .address_space:  global
        .offset:         16
        .size:           8
        .value_kind:     global_buffer
      - .actual_access:  write_only
        .address_space:  global
        .offset:         24
        .size:           8
        .value_kind:     global_buffer
      - .actual_access:  write_only
        .address_space:  global
        .offset:         32
        .size:           8
        .value_kind:     global_buffer
      - .actual_access:  write_only
        .address_space:  global
        .offset:         40
        .size:           8
        .value_kind:     global_buffer
    .group_segment_fixed_size: 100880
    .kernarg_segment_align: 8
    .kernarg_segment_size: 48
    .language:       OpenCL C
    .language_version:
      - 2
      - 0
    .max_flat_workgroup_size: 768
    .name:           _Z14seg_sum_kernelPKfS0_S0_PDv8_DF16bS2_Pf
    .private_segment_fixed_size: 0
    .sgpr_count:     42
    .sgpr_spill_count: 0
    .symbol:         _Z14seg_sum_kernelPKfS0_S0_PDv8_DF16bS2_Pf.kd
    .uniform_work_group_size: 1
    .uses_dynamic_stack: false
    .vgpr_count:     142
    .vgpr_spill_count: 0
    .wavefront_size: 64
  - .agpr_count:     16
    .args:
      - .actual_access:  read_only
        .address_space:  global
        .offset:         0
        .size:           8
        .value_kind:     global_buffer
      - .actual_access:  read_only
        .address_space:  global
        .offset:         8
        .size:           8
        .value_kind:     global_buffer
      - .actual_access:  read_only
        .address_space:  global
        .offset:         16
        .size:           8
        .value_kind:     global_buffer
      - .actual_access:  read_only
        .address_space:  global
        .offset:         24
        .size:           8
        .value_kind:     global_buffer
      - .actual_access:  write_only
        .address_space:  global
        .offset:         32
        .size:           8
        .value_kind:     global_buffer
      - .actual_access:  write_only
        .address_space:  global
        .offset:         40
        .size:           8
        .value_kind:     global_buffer
      - .actual_access:  write_only
        .address_space:  global
        .offset:         48
        .size:           8
        .value_kind:     global_buffer
    .group_segment_fixed_size: 17152
    .kernarg_segment_align: 8
    .kernarg_segment_size: 56
    .language:       OpenCL C
    .language_version:
      - 2
      - 0
    .max_flat_workgroup_size: 256
    .name:           _Z13logits_kernelPKDv8_DF16bS1_PKfS3_PDv2_fS5_Pf
    .private_segment_fixed_size: 0
    .sgpr_count:     37
    .sgpr_spill_count: 0
    .symbol:         _Z13logits_kernelPKDv8_DF16bS1_PKfS3_PDv2_fS5_Pf.kd
    .uniform_work_group_size: 1
    .uses_dynamic_stack: false
    .vgpr_count:     268
    .vgpr_spill_count: 0
    .wavefront_size: 64
  - .agpr_count:     0
    .args:
      - .actual_access:  read_only
        .address_space:  global
        .offset:         0
        .size:           8
        .value_kind:     global_buffer
      - .actual_access:  read_only
        .address_space:  global
        .offset:         8
        .size:           8
        .value_kind:     global_buffer
      - .actual_access:  read_only
        .address_space:  global
        .offset:         16
        .size:           8
        .value_kind:     global_buffer
      - .actual_access:  read_only
        .address_space:  global
        .offset:         24
        .size:           8
        .value_kind:     global_buffer
      - .actual_access:  write_only
        .address_space:  global
        .offset:         32
        .size:           8
        .value_kind:     global_buffer
    .group_segment_fixed_size: 128
    .kernarg_segment_align: 8
    .kernarg_segment_size: 40
    .language:       OpenCL C
    .language_version:
      - 2
      - 0
    .max_flat_workgroup_size: 1024
    .name:           _Z12final_kernelPKDv4_fS1_PKfS3_Pf
    .private_segment_fixed_size: 0
    .sgpr_count:     20
    .sgpr_spill_count: 0
    .symbol:         _Z12final_kernelPKDv4_fS1_PKfS3_Pf.kd
    .uniform_work_group_size: 1
    .uses_dynamic_stack: false
    .vgpr_count:     52
    .vgpr_spill_count: 0
    .wavefront_size: 64
